# final rmsnorm sweep rewritten by hand as a two-bank software pipeline (next token's 12 row loads in flight under the current token's reduction and stores)
# speedup vs baseline: 1.0036x; 1.0036x over previous
.LBB0_1120:
	v_lshl_add_u64 v[54:55], v[52:53], 0, s[8:9]
	v_add_co_u32_e32 v54, vcc, 0x80000000, v54
	s_nop 1
	v_addc_co_u32_e32 v55, vcc, 0, v55, vcc
	v_lshl_add_u64 v[56:57], v[48:49], 0, s[8:9]
	s_mov_b64 s[24:25], 0x1000
	s_mov_b32 s30, s2
	v_lshl_add_u64 v[252:253], v[54:55], 0, s[24:25]
	global_load_dwordx4 v[102:105], v[50:51], off
	global_load_dwordx4 v[106:109], v[50:51], off offset:16
	global_load_dwordx4 v[110:113], v[50:51], off offset:2048
	global_load_dwordx4 v[114:117], v[50:51], off offset:2064
	global_load_dwordx4 v[118:121], v[54:55], off
	global_load_dwordx4 v[122:125], v[54:55], off offset:2048
	global_load_dwordx4 v[126:129], v[252:253], off
	global_load_dwordx4 v[130:133], v[252:253], off offset:2048
	global_load_dwordx4 v[134:137], v[54:55], off offset:1024
	global_load_dwordx4 v[138:141], v[54:55], off offset:3072
	global_load_dwordx4 v[142:145], v[252:253], off offset:1024
	global_load_dwordx4 v[146:149], v[252:253], off offset:3072
.Lp8_top:
	s_add_i32 s31, s30, s4
	s_cmp_lt_i32 s31, 0x8000
	s_cselect_b32 s30, s31, s30
	s_cselect_b32 s26, s6, 0
	s_cselect_b32 s27, s7, 0
	s_cselect_b32 s28, s10, 0
	s_cselect_b32 s29, s11, 0
	v_lshl_add_u64 v[50:51], v[50:51], 0, s[26:27]
	v_lshl_add_u64 v[54:55], v[54:55], 0, s[28:29]
	v_lshl_add_u64 v[252:253], v[54:55], 0, s[24:25]
	global_load_dwordx4 v[150:153], v[50:51], off
	global_load_dwordx4 v[154:157], v[50:51], off offset:16
	global_load_dwordx4 v[158:161], v[50:51], off offset:2048
	global_load_dwordx4 v[162:165], v[50:51], off offset:2064
	global_load_dwordx4 v[166:169], v[54:55], off
	global_load_dwordx4 v[170:173], v[54:55], off offset:2048
	global_load_dwordx4 v[174:177], v[252:253], off
	global_load_dwordx4 v[178:181], v[252:253], off offset:2048
	global_load_dwordx4 v[182:185], v[54:55], off offset:1024
	global_load_dwordx4 v[186:189], v[54:55], off offset:3072
	global_load_dwordx4 v[190:193], v[252:253], off offset:1024
	global_load_dwordx4 v[194:197], v[252:253], off offset:3072
	s_cmpk_gt_i32 s2, 0x3fff
	s_cselect_b32 s12, 0x2000, 0
	v_add_u32_e32 v69, s12, v66
	ds_read_b128 v[70:73], v69
	ds_read_b128 v[74:77], v69 offset:16
	ds_read_b128 v[78:81], v69 offset:32
	ds_read_b128 v[82:85], v69 offset:48
	ds_read_b128 v[86:89], v69 offset:4096
	ds_read_b128 v[90:93], v69 offset:4112
	ds_read_b128 v[94:97], v69 offset:4128
	ds_read_b128 v[98:101], v69 offset:4144
	v_lshl_add_u64 v[58:59], v[56:57], 0, s[24:25]
	s_waitcnt vmcnt(12)
	s_waitcnt lgkmcnt(0)
	v_cvt_pk_f32_fp8_e32 v[230:231], v118
	v_cvt_pk_f32_fp8_sdwa v[238:239], v118 src0_sel:WORD_1
	v_cvt_pk_f32_fp8_e32 v[232:233], v122
	v_cvt_pk_f32_fp8_sdwa v[240:241], v122 src0_sel:WORD_1
	v_cvt_pk_f32_fp8_e32 v[234:235], v126
	v_cvt_pk_f32_fp8_sdwa v[242:243], v126 src0_sel:WORD_1
	v_cvt_pk_f32_fp8_e32 v[236:237], v130
	v_cvt_pk_f32_fp8_sdwa v[244:245], v130 src0_sel:WORD_1
	v_lshlrev_b32_e32 v246, 16, v102
	v_and_b32_e32 v247, 0xffff0000, v102
	v_lshlrev_b32_e32 v248, 16, v103
	v_and_b32_e32 v249, 0xffff0000, v103
	v_pk_add_f32 v[230:231], v[230:231], v[232:233]
	v_pk_add_f32 v[234:235], v[234:235], v[236:237]
	v_pk_add_f32 v[238:239], v[238:239], v[240:241]
	v_pk_add_f32 v[242:243], v[242:243], v[244:245]
	v_pk_add_f32 v[230:231], v[230:231], v[234:235]
	v_pk_add_f32 v[238:239], v[238:239], v[242:243]
	v_pk_fma_f32 v[198:199], v[70:71], v[230:231], v[246:247]
	v_pk_fma_f32 v[200:201], v[72:73], v[238:239], v[248:249]
	v_pk_mul_f32 v[250:251], v[198:199], v[198:199]
	v_pk_fma_f32 v[250:251], v[200:201], v[200:201], v[250:251]
	v_cvt_pk_f32_fp8_e32 v[230:231], v119
	v_cvt_pk_f32_fp8_sdwa v[238:239], v119 src0_sel:WORD_1
	v_cvt_pk_f32_fp8_e32 v[232:233], v123
	v_cvt_pk_f32_fp8_sdwa v[240:241], v123 src0_sel:WORD_1
	v_cvt_pk_f32_fp8_e32 v[234:235], v127
	v_cvt_pk_f32_fp8_sdwa v[242:243], v127 src0_sel:WORD_1
	v_cvt_pk_f32_fp8_e32 v[236:237], v131
	v_cvt_pk_f32_fp8_sdwa v[244:245], v131 src0_sel:WORD_1
	v_lshlrev_b32_e32 v246, 16, v104
	v_and_b32_e32 v247, 0xffff0000, v104
	v_lshlrev_b32_e32 v248, 16, v105
	v_and_b32_e32 v249, 0xffff0000, v105
	v_pk_add_f32 v[230:231], v[230:231], v[232:233]
	v_pk_add_f32 v[234:235], v[234:235], v[236:237]
	v_pk_add_f32 v[238:239], v[238:239], v[240:241]
	v_pk_add_f32 v[242:243], v[242:243], v[244:245]
	v_pk_add_f32 v[230:231], v[230:231], v[234:235]
	v_pk_add_f32 v[238:239], v[238:239], v[242:243]
	v_pk_fma_f32 v[202:203], v[74:75], v[230:231], v[246:247]
	v_pk_fma_f32 v[204:205], v[76:77], v[238:239], v[248:249]
	v_pk_fma_f32 v[250:251], v[202:203], v[202:203], v[250:251]
	v_pk_fma_f32 v[250:251], v[204:205], v[204:205], v[250:251]
	v_cvt_pk_f32_fp8_e32 v[230:231], v120
	v_cvt_pk_f32_fp8_sdwa v[238:239], v120 src0_sel:WORD_1
	v_cvt_pk_f32_fp8_e32 v[232:233], v124
	v_cvt_pk_f32_fp8_sdwa v[240:241], v124 src0_sel:WORD_1
	v_cvt_pk_f32_fp8_e32 v[234:235], v128
	v_cvt_pk_f32_fp8_sdwa v[242:243], v128 src0_sel:WORD_1
	v_cvt_pk_f32_fp8_e32 v[236:237], v132
	v_cvt_pk_f32_fp8_sdwa v[244:245], v132 src0_sel:WORD_1
	v_lshlrev_b32_e32 v246, 16, v106
	v_and_b32_e32 v247, 0xffff0000, v106
	v_lshlrev_b32_e32 v248, 16, v107
	v_and_b32_e32 v249, 0xffff0000, v107
	v_pk_add_f32 v[230:231], v[230:231], v[232:233]
	v_pk_add_f32 v[234:235], v[234:235], v[236:237]
	v_pk_add_f32 v[238:239], v[238:239], v[240:241]
	v_pk_add_f32 v[242:243], v[242:243], v[244:245]
	v_pk_add_f32 v[230:231], v[230:231], v[234:235]
	v_pk_add_f32 v[238:239], v[238:239], v[242:243]
	v_pk_fma_f32 v[206:207], v[78:79], v[230:231], v[246:247]
	v_pk_fma_f32 v[208:209], v[80:81], v[238:239], v[248:249]
	v_pk_fma_f32 v[250:251], v[206:207], v[206:207], v[250:251]
	v_pk_fma_f32 v[250:251], v[208:209], v[208:209], v[250:251]
	v_cvt_pk_f32_fp8_e32 v[230:231], v121
	v_cvt_pk_f32_fp8_sdwa v[238:239], v121 src0_sel:WORD_1
	v_cvt_pk_f32_fp8_e32 v[232:233], v125
	v_cvt_pk_f32_fp8_sdwa v[240:241], v125 src0_sel:WORD_1
	v_cvt_pk_f32_fp8_e32 v[234:235], v129
	v_cvt_pk_f32_fp8_sdwa v[242:243], v129 src0_sel:WORD_1
	v_cvt_pk_f32_fp8_e32 v[236:237], v133
	v_cvt_pk_f32_fp8_sdwa v[244:245], v133 src0_sel:WORD_1
	v_lshlrev_b32_e32 v246, 16, v108
	v_and_b32_e32 v247, 0xffff0000, v108
	v_lshlrev_b32_e32 v248, 16, v109
	v_and_b32_e32 v249, 0xffff0000, v109
	v_pk_add_f32 v[230:231], v[230:231], v[232:233]
	v_pk_add_f32 v[234:235], v[234:235], v[236:237]
	v_pk_add_f32 v[238:239], v[238:239], v[240:241]
	v_pk_add_f32 v[242:243], v[242:243], v[244:245]
	v_pk_add_f32 v[230:231], v[230:231], v[234:235]
	v_pk_add_f32 v[238:239], v[238:239], v[242:243]
	v_pk_fma_f32 v[210:211], v[82:83], v[230:231], v[246:247]
	v_pk_fma_f32 v[212:213], v[84:85], v[238:239], v[248:249]
	v_pk_fma_f32 v[250:251], v[210:211], v[210:211], v[250:251]
	v_pk_fma_f32 v[250:251], v[212:213], v[212:213], v[250:251]
	v_cvt_pk_f32_fp8_e32 v[230:231], v134
	v_cvt_pk_f32_fp8_sdwa v[238:239], v134 src0_sel:WORD_1
	v_cvt_pk_f32_fp8_e32 v[232:233], v138
	v_cvt_pk_f32_fp8_sdwa v[240:241], v138 src0_sel:WORD_1
	v_cvt_pk_f32_fp8_e32 v[234:235], v142
	v_cvt_pk_f32_fp8_sdwa v[242:243], v142 src0_sel:WORD_1
	v_cvt_pk_f32_fp8_e32 v[236:237], v146
	v_cvt_pk_f32_fp8_sdwa v[244:245], v146 src0_sel:WORD_1
	v_lshlrev_b32_e32 v246, 16, v110
	v_and_b32_e32 v247, 0xffff0000, v110
	v_lshlrev_b32_e32 v248, 16, v111
	v_and_b32_e32 v249, 0xffff0000, v111
	v_pk_add_f32 v[230:231], v[230:231], v[232:233]
	v_pk_add_f32 v[234:235], v[234:235], v[236:237]
	v_pk_add_f32 v[238:239], v[238:239], v[240:241]
	v_pk_add_f32 v[242:243], v[242:243], v[244:245]
	v_pk_add_f32 v[230:231], v[230:231], v[234:235]
	v_pk_add_f32 v[238:239], v[238:239], v[242:243]
	v_pk_fma_f32 v[214:215], v[86:87], v[230:231], v[246:247]
	v_pk_fma_f32 v[216:217], v[88:89], v[238:239], v[248:249]
	v_pk_fma_f32 v[250:251], v[214:215], v[214:215], v[250:251]
	v_pk_fma_f32 v[250:251], v[216:217], v[216:217], v[250:251]
	v_cvt_pk_f32_fp8_e32 v[230:231], v135
	v_cvt_pk_f32_fp8_sdwa v[238:239], v135 src0_sel:WORD_1
	v_cvt_pk_f32_fp8_e32 v[232:233], v139
	v_cvt_pk_f32_fp8_sdwa v[240:241], v139 src0_sel:WORD_1
	v_cvt_pk_f32_fp8_e32 v[234:235], v143
	v_cvt_pk_f32_fp8_sdwa v[242:243], v143 src0_sel:WORD_1
	v_cvt_pk_f32_fp8_e32 v[236:237], v147
	v_cvt_pk_f32_fp8_sdwa v[244:245], v147 src0_sel:WORD_1
	v_lshlrev_b32_e32 v246, 16, v112
	v_and_b32_e32 v247, 0xffff0000, v112
	v_lshlrev_b32_e32 v248, 16, v113
	v_and_b32_e32 v249, 0xffff0000, v113
	v_pk_add_f32 v[230:231], v[230:231], v[232:233]
	v_pk_add_f32 v[234:235], v[234:235], v[236:237]
	v_pk_add_f32 v[238:239], v[238:239], v[240:241]
	v_pk_add_f32 v[242:243], v[242:243], v[244:245]
	v_pk_add_f32 v[230:231], v[230:231], v[234:235]
	v_pk_add_f32 v[238:239], v[238:239], v[242:243]
	v_pk_fma_f32 v[218:219], v[90:91], v[230:231], v[246:247]
	v_pk_fma_f32 v[220:221], v[92:93], v[238:239], v[248:249]
	v_pk_fma_f32 v[250:251], v[218:219], v[218:219], v[250:251]
	v_pk_fma_f32 v[250:251], v[220:221], v[220:221], v[250:251]
	v_cvt_pk_f32_fp8_e32 v[230:231], v136
	v_cvt_pk_f32_fp8_sdwa v[238:239], v136 src0_sel:WORD_1
	v_cvt_pk_f32_fp8_e32 v[232:233], v140
	v_cvt_pk_f32_fp8_sdwa v[240:241], v140 src0_sel:WORD_1
	v_cvt_pk_f32_fp8_e32 v[234:235], v144
	v_cvt_pk_f32_fp8_sdwa v[242:243], v144 src0_sel:WORD_1
	v_cvt_pk_f32_fp8_e32 v[236:237], v148
	v_cvt_pk_f32_fp8_sdwa v[244:245], v148 src0_sel:WORD_1
	v_lshlrev_b32_e32 v246, 16, v114
	v_and_b32_e32 v247, 0xffff0000, v114
	v_lshlrev_b32_e32 v248, 16, v115
	v_and_b32_e32 v249, 0xffff0000, v115
	v_pk_add_f32 v[230:231], v[230:231], v[232:233]
	v_pk_add_f32 v[234:235], v[234:235], v[236:237]
	v_pk_add_f32 v[238:239], v[238:239], v[240:241]
	v_pk_add_f32 v[242:243], v[242:243], v[244:245]
	v_pk_add_f32 v[230:231], v[230:231], v[234:235]
	v_pk_add_f32 v[238:239], v[238:239], v[242:243]
	v_pk_fma_f32 v[222:223], v[94:95], v[230:231], v[246:247]
	v_pk_fma_f32 v[224:225], v[96:97], v[238:239], v[248:249]
	v_pk_fma_f32 v[250:251], v[222:223], v[222:223], v[250:251]
	v_pk_fma_f32 v[250:251], v[224:225], v[224:225], v[250:251]
	v_cvt_pk_f32_fp8_e32 v[230:231], v137
	v_cvt_pk_f32_fp8_sdwa v[238:239], v137 src0_sel:WORD_1
	v_cvt_pk_f32_fp8_e32 v[232:233], v141
	v_cvt_pk_f32_fp8_sdwa v[240:241], v141 src0_sel:WORD_1
	v_cvt_pk_f32_fp8_e32 v[234:235], v145
	v_cvt_pk_f32_fp8_sdwa v[242:243], v145 src0_sel:WORD_1
	v_cvt_pk_f32_fp8_e32 v[236:237], v149
	v_cvt_pk_f32_fp8_sdwa v[244:245], v149 src0_sel:WORD_1
	v_lshlrev_b32_e32 v246, 16, v116
	v_and_b32_e32 v247, 0xffff0000, v116
	v_lshlrev_b32_e32 v248, 16, v117
	v_and_b32_e32 v249, 0xffff0000, v117
	v_pk_add_f32 v[230:231], v[230:231], v[232:233]
	v_pk_add_f32 v[234:235], v[234:235], v[236:237]
	v_pk_add_f32 v[238:239], v[238:239], v[240:241]
	v_pk_add_f32 v[242:243], v[242:243], v[244:245]
	v_pk_add_f32 v[230:231], v[230:231], v[234:235]
	v_pk_add_f32 v[238:239], v[238:239], v[242:243]
	v_pk_fma_f32 v[226:227], v[98:99], v[230:231], v[246:247]
	v_pk_fma_f32 v[228:229], v[100:101], v[238:239], v[248:249]
	v_pk_fma_f32 v[250:251], v[226:227], v[226:227], v[250:251]
	v_pk_fma_f32 v[250:251], v[228:229], v[228:229], v[250:251]
	s_nop 0
	v_add_f32_e32 v69, v250, v251
	ds_bpermute_b32 v230, v60, v69
	s_waitcnt lgkmcnt(0)
	v_add_f32_e32 v69, v69, v230
	ds_bpermute_b32 v230, v61, v69
	s_waitcnt lgkmcnt(0)
	v_add_f32_e32 v69, v69, v230
	ds_bpermute_b32 v230, v62, v69
	s_waitcnt lgkmcnt(0)
	v_add_f32_e32 v69, v69, v230
	ds_bpermute_b32 v230, v63, v69
	s_waitcnt lgkmcnt(0)
	v_add_f32_e32 v69, v69, v230
	ds_bpermute_b32 v230, v64, v69
	s_waitcnt lgkmcnt(0)
	v_add_f32_e32 v69, v69, v230
	ds_bpermute_b32 v230, v65, v69
	s_waitcnt lgkmcnt(0)
	v_add_f32_e32 v69, v69, v230
	v_fmamk_f32 v69, v69, 0x3a000000, v67
	v_mul_f32_e32 v230, 0x4f800000, v69
	v_cmp_gt_f32_e32 vcc, s3, v69
	s_nop 1
	v_cndmask_b32_e32 v69, v69, v230, vcc
	v_sqrt_f32_e32 v230, v69
	s_nop 0
	v_add_u32_e32 v231, -1, v230
	v_add_u32_e32 v232, 1, v230
	v_fma_f32 v233, -v231, v230, v69
	v_fma_f32 v234, -v232, v230, v69
	v_cmp_ge_f32_e64 s[0:1], 0, v233
	s_nop 1
	v_cndmask_b32_e64 v230, v230, v231, s[0:1]
	v_cmp_lt_f32_e64 s[0:1], 0, v234
	s_nop 1
	v_cndmask_b32_e64 v230, v230, v232, s[0:1]
	v_mul_f32_e32 v231, 0x37800000, v230
	v_cndmask_b32_e32 v230, v230, v231, vcc
	v_cmp_class_f32_e32 vcc, v69, v68
	s_nop 1
	v_cndmask_b32_e32 v69, v230, v69, vcc
	v_div_scale_f32 v230, s[0:1], v69, v69, 1.0
	v_rcp_f32_e32 v232, v230
	v_div_scale_f32 v231, vcc, 1.0, v69, 1.0
	v_fma_f32 v233, -v230, v232, 1.0
	v_fmac_f32_e32 v232, v233, v232
	v_mul_f32_e32 v233, v231, v232
	v_fma_f32 v234, -v230, v233, v231
	v_fmac_f32_e32 v233, v234, v232
	v_fma_f32 v230, -v230, v233, v231
	v_div_fmas_f32 v230, v230, v232, v233
	v_div_fixup_f32 v230, v230, v69, 1.0
	v_pk_mul_f32 v[198:199], v[198:199], v[230:231] op_sel_hi:[1,0]
	v_pk_mul_f32 v[200:201], v[200:201], v[230:231] op_sel_hi:[1,0]
	v_pk_mul_f32 v[202:203], v[202:203], v[230:231] op_sel_hi:[1,0]
	v_pk_mul_f32 v[204:205], v[204:205], v[230:231] op_sel_hi:[1,0]
	v_pk_mul_f32 v[206:207], v[206:207], v[230:231] op_sel_hi:[1,0]
	v_pk_mul_f32 v[208:209], v[208:209], v[230:231] op_sel_hi:[1,0]
	v_pk_mul_f32 v[210:211], v[210:211], v[230:231] op_sel_hi:[1,0]
	v_pk_mul_f32 v[212:213], v[212:213], v[230:231] op_sel_hi:[1,0]
	v_pk_mul_f32 v[214:215], v[214:215], v[230:231] op_sel_hi:[1,0]
	v_pk_mul_f32 v[216:217], v[216:217], v[230:231] op_sel_hi:[1,0]
	v_pk_mul_f32 v[218:219], v[218:219], v[230:231] op_sel_hi:[1,0]
	v_pk_mul_f32 v[220:221], v[220:221], v[230:231] op_sel_hi:[1,0]
	v_pk_mul_f32 v[222:223], v[222:223], v[230:231] op_sel_hi:[1,0]
	v_pk_mul_f32 v[224:225], v[224:225], v[230:231] op_sel_hi:[1,0]
	v_pk_mul_f32 v[226:227], v[226:227], v[230:231] op_sel_hi:[1,0]
	v_pk_mul_f32 v[228:229], v[228:229], v[230:231] op_sel_hi:[1,0]
	v_pk_mul_f32 v[198:199], v[0:1], v[198:199]
	v_pk_mul_f32 v[200:201], v[2:3], v[200:201]
	v_pk_mul_f32 v[202:203], v[4:5], v[202:203]
	v_pk_mul_f32 v[204:205], v[6:7], v[204:205]
	v_pk_mul_f32 v[206:207], v[8:9], v[206:207]
	v_pk_mul_f32 v[208:209], v[10:11], v[208:209]
	v_pk_mul_f32 v[210:211], v[12:13], v[210:211]
	v_pk_mul_f32 v[212:213], v[14:15], v[212:213]
	v_pk_mul_f32 v[214:215], v[16:17], v[214:215]
	v_pk_mul_f32 v[216:217], v[18:19], v[216:217]
	v_pk_mul_f32 v[218:219], v[20:21], v[218:219]
	v_pk_mul_f32 v[220:221], v[22:23], v[220:221]
	v_pk_mul_f32 v[222:223], v[24:25], v[222:223]
	v_pk_mul_f32 v[224:225], v[26:27], v[224:225]
	v_pk_mul_f32 v[226:227], v[28:29], v[226:227]
	v_pk_mul_f32 v[228:229], v[30:31], v[228:229]
	global_store_dwordx4 v[56:57], v[198:201], off
	global_store_dwordx4 v[56:57], v[202:205], off offset:16
	global_store_dwordx4 v[56:57], v[206:209], off offset:32
	global_store_dwordx4 v[56:57], v[210:213], off offset:48
	global_store_dwordx4 v[58:59], v[214:217], off
	global_store_dwordx4 v[58:59], v[218:221], off offset:16
	global_store_dwordx4 v[58:59], v[222:225], off offset:32
	global_store_dwordx4 v[58:59], v[226:229], off offset:48
	v_lshl_add_u64 v[56:57], v[56:57], 0, s[10:11]
	s_add_i32 s2, s2, s4
	s_cmp_lt_i32 s2, 0x8000
	s_cbranch_scc0 .Lp8_done
	s_add_i32 s31, s30, s4
	s_cmp_lt_i32 s31, 0x8000
	s_cselect_b32 s30, s31, s30
	s_cselect_b32 s26, s6, 0
	s_cselect_b32 s27, s7, 0
	s_cselect_b32 s28, s10, 0
	s_cselect_b32 s29, s11, 0
	v_lshl_add_u64 v[50:51], v[50:51], 0, s[26:27]
	v_lshl_add_u64 v[54:55], v[54:55], 0, s[28:29]
	v_lshl_add_u64 v[252:253], v[54:55], 0, s[24:25]
	global_load_dwordx4 v[102:105], v[50:51], off
	global_load_dwordx4 v[106:109], v[50:51], off offset:16
	global_load_dwordx4 v[110:113], v[50:51], off offset:2048
	global_load_dwordx4 v[114:117], v[50:51], off offset:2064
	global_load_dwordx4 v[118:121], v[54:55], off
	global_load_dwordx4 v[122:125], v[54:55], off offset:2048
	global_load_dwordx4 v[126:129], v[252:253], off
	global_load_dwordx4 v[130:133], v[252:253], off offset:2048
	global_load_dwordx4 v[134:137], v[54:55], off offset:1024
	global_load_dwordx4 v[138:141], v[54:55], off offset:3072
	global_load_dwordx4 v[142:145], v[252:253], off offset:1024
	global_load_dwordx4 v[146:149], v[252:253], off offset:3072
	s_cmpk_gt_i32 s2, 0x3fff
	s_cselect_b32 s12, 0x2000, 0
	v_add_u32_e32 v69, s12, v66
	ds_read_b128 v[70:73], v69
	ds_read_b128 v[74:77], v69 offset:16
	ds_read_b128 v[78:81], v69 offset:32
	ds_read_b128 v[82:85], v69 offset:48
	ds_read_b128 v[86:89], v69 offset:4096
	ds_read_b128 v[90:93], v69 offset:4112
	ds_read_b128 v[94:97], v69 offset:4128
	ds_read_b128 v[98:101], v69 offset:4144
	v_lshl_add_u64 v[58:59], v[56:57], 0, s[24:25]
	s_waitcnt vmcnt(12)
	s_waitcnt lgkmcnt(0)
	v_cvt_pk_f32_fp8_e32 v[230:231], v166
	v_cvt_pk_f32_fp8_sdwa v[238:239], v166 src0_sel:WORD_1
	v_cvt_pk_f32_fp8_e32 v[232:233], v170
	v_cvt_pk_f32_fp8_sdwa v[240:241], v170 src0_sel:WORD_1
	v_cvt_pk_f32_fp8_e32 v[234:235], v174
	v_cvt_pk_f32_fp8_sdwa v[242:243], v174 src0_sel:WORD_1
	v_cvt_pk_f32_fp8_e32 v[236:237], v178
	v_cvt_pk_f32_fp8_sdwa v[244:245], v178 src0_sel:WORD_1
	v_lshlrev_b32_e32 v246, 16, v150
	v_and_b32_e32 v247, 0xffff0000, v150
	v_lshlrev_b32_e32 v248, 16, v151
	v_and_b32_e32 v249, 0xffff0000, v151
	v_pk_add_f32 v[230:231], v[230:231], v[232:233]
	v_pk_add_f32 v[234:235], v[234:235], v[236:237]
	v_pk_add_f32 v[238:239], v[238:239], v[240:241]
	v_pk_add_f32 v[242:243], v[242:243], v[244:245]
	v_pk_add_f32 v[230:231], v[230:231], v[234:235]
	v_pk_add_f32 v[238:239], v[238:239], v[242:243]
	v_pk_fma_f32 v[198:199], v[70:71], v[230:231], v[246:247]
	v_pk_fma_f32 v[200:201], v[72:73], v[238:239], v[248:249]
	v_pk_mul_f32 v[250:251], v[198:199], v[198:199]
	v_pk_fma_f32 v[250:251], v[200:201], v[200:201], v[250:251]
	v_cvt_pk_f32_fp8_e32 v[230:231], v167
	v_cvt_pk_f32_fp8_sdwa v[238:239], v167 src0_sel:WORD_1
	v_cvt_pk_f32_fp8_e32 v[232:233], v171
	v_cvt_pk_f32_fp8_sdwa v[240:241], v171 src0_sel:WORD_1
	v_cvt_pk_f32_fp8_e32 v[234:235], v175
	v_cvt_pk_f32_fp8_sdwa v[242:243], v175 src0_sel:WORD_1
	v_cvt_pk_f32_fp8_e32 v[236:237], v179
	v_cvt_pk_f32_fp8_sdwa v[244:245], v179 src0_sel:WORD_1
	v_lshlrev_b32_e32 v246, 16, v152
	v_and_b32_e32 v247, 0xffff0000, v152
	v_lshlrev_b32_e32 v248, 16, v153
	v_and_b32_e32 v249, 0xffff0000, v153
	v_pk_add_f32 v[230:231], v[230:231], v[232:233]
	v_pk_add_f32 v[234:235], v[234:235], v[236:237]
	v_pk_add_f32 v[238:239], v[238:239], v[240:241]
	v_pk_add_f32 v[242:243], v[242:243], v[244:245]
	v_pk_add_f32 v[230:231], v[230:231], v[234:235]
	v_pk_add_f32 v[238:239], v[238:239], v[242:243]
	v_pk_fma_f32 v[202:203], v[74:75], v[230:231], v[246:247]
	v_pk_fma_f32 v[204:205], v[76:77], v[238:239], v[248:249]
	v_pk_fma_f32 v[250:251], v[202:203], v[202:203], v[250:251]
	v_pk_fma_f32 v[250:251], v[204:205], v[204:205], v[250:251]
	v_cvt_pk_f32_fp8_e32 v[230:231], v168
	v_cvt_pk_f32_fp8_sdwa v[238:239], v168 src0_sel:WORD_1
	v_cvt_pk_f32_fp8_e32 v[232:233], v172
	v_cvt_pk_f32_fp8_sdwa v[240:241], v172 src0_sel:WORD_1
	v_cvt_pk_f32_fp8_e32 v[234:235], v176
	v_cvt_pk_f32_fp8_sdwa v[242:243], v176 src0_sel:WORD_1
	v_cvt_pk_f32_fp8_e32 v[236:237], v180
	v_cvt_pk_f32_fp8_sdwa v[244:245], v180 src0_sel:WORD_1
	v_lshlrev_b32_e32 v246, 16, v154
	v_and_b32_e32 v247, 0xffff0000, v154
	v_lshlrev_b32_e32 v248, 16, v155
	v_and_b32_e32 v249, 0xffff0000, v155
	v_pk_add_f32 v[230:231], v[230:231], v[232:233]
	v_pk_add_f32 v[234:235], v[234:235], v[236:237]
	v_pk_add_f32 v[238:239], v[238:239], v[240:241]
	v_pk_add_f32 v[242:243], v[242:243], v[244:245]
	v_pk_add_f32 v[230:231], v[230:231], v[234:235]
	v_pk_add_f32 v[238:239], v[238:239], v[242:243]
	v_pk_fma_f32 v[206:207], v[78:79], v[230:231], v[246:247]
	v_pk_fma_f32 v[208:209], v[80:81], v[238:239], v[248:249]
	v_pk_fma_f32 v[250:251], v[206:207], v[206:207], v[250:251]
	v_pk_fma_f32 v[250:251], v[208:209], v[208:209], v[250:251]
	v_cvt_pk_f32_fp8_e32 v[230:231], v169
	v_cvt_pk_f32_fp8_sdwa v[238:239], v169 src0_sel:WORD_1
	v_cvt_pk_f32_fp8_e32 v[232:233], v173
	v_cvt_pk_f32_fp8_sdwa v[240:241], v173 src0_sel:WORD_1
	v_cvt_pk_f32_fp8_e32 v[234:235], v177
	v_cvt_pk_f32_fp8_sdwa v[242:243], v177 src0_sel:WORD_1
	v_cvt_pk_f32_fp8_e32 v[236:237], v181
	v_cvt_pk_f32_fp8_sdwa v[244:245], v181 src0_sel:WORD_1
	v_lshlrev_b32_e32 v246, 16, v156
	v_and_b32_e32 v247, 0xffff0000, v156
	v_lshlrev_b32_e32 v248, 16, v157
	v_and_b32_e32 v249, 0xffff0000, v157
	v_pk_add_f32 v[230:231], v[230:231], v[232:233]
	v_pk_add_f32 v[234:235], v[234:235], v[236:237]
	v_pk_add_f32 v[238:239], v[238:239], v[240:241]
	v_pk_add_f32 v[242:243], v[242:243], v[244:245]
	v_pk_add_f32 v[230:231], v[230:231], v[234:235]
	v_pk_add_f32 v[238:239], v[238:239], v[242:243]
	v_pk_fma_f32 v[210:211], v[82:83], v[230:231], v[246:247]
	v_pk_fma_f32 v[212:213], v[84:85], v[238:239], v[248:249]
	v_pk_fma_f32 v[250:251], v[210:211], v[210:211], v[250:251]
	v_pk_fma_f32 v[250:251], v[212:213], v[212:213], v[250:251]
	v_cvt_pk_f32_fp8_e32 v[230:231], v182
	v_cvt_pk_f32_fp8_sdwa v[238:239], v182 src0_sel:WORD_1
	v_cvt_pk_f32_fp8_e32 v[232:233], v186
	v_cvt_pk_f32_fp8_sdwa v[240:241], v186 src0_sel:WORD_1
	v_cvt_pk_f32_fp8_e32 v[234:235], v190
	v_cvt_pk_f32_fp8_sdwa v[242:243], v190 src0_sel:WORD_1
	v_cvt_pk_f32_fp8_e32 v[236:237], v194
	v_cvt_pk_f32_fp8_sdwa v[244:245], v194 src0_sel:WORD_1
	v_lshlrev_b32_e32 v246, 16, v158
	v_and_b32_e32 v247, 0xffff0000, v158
	v_lshlrev_b32_e32 v248, 16, v159
	v_and_b32_e32 v249, 0xffff0000, v159
	v_pk_add_f32 v[230:231], v[230:231], v[232:233]
	v_pk_add_f32 v[234:235], v[234:235], v[236:237]
	v_pk_add_f32 v[238:239], v[238:239], v[240:241]
	v_pk_add_f32 v[242:243], v[242:243], v[244:245]
	v_pk_add_f32 v[230:231], v[230:231], v[234:235]
	v_pk_add_f32 v[238:239], v[238:239], v[242:243]
	v_pk_fma_f32 v[214:215], v[86:87], v[230:231], v[246:247]
	v_pk_fma_f32 v[216:217], v[88:89], v[238:239], v[248:249]
	v_pk_fma_f32 v[250:251], v[214:215], v[214:215], v[250:251]
	v_pk_fma_f32 v[250:251], v[216:217], v[216:217], v[250:251]
	v_cvt_pk_f32_fp8_e32 v[230:231], v183
	v_cvt_pk_f32_fp8_sdwa v[238:239], v183 src0_sel:WORD_1
	v_cvt_pk_f32_fp8_e32 v[232:233], v187
	v_cvt_pk_f32_fp8_sdwa v[240:241], v187 src0_sel:WORD_1
	v_cvt_pk_f32_fp8_e32 v[234:235], v191
	v_cvt_pk_f32_fp8_sdwa v[242:243], v191 src0_sel:WORD_1
	v_cvt_pk_f32_fp8_e32 v[236:237], v195
	v_cvt_pk_f32_fp8_sdwa v[244:245], v195 src0_sel:WORD_1
	v_lshlrev_b32_e32 v246, 16, v160
	v_and_b32_e32 v247, 0xffff0000, v160
	v_lshlrev_b32_e32 v248, 16, v161
	v_and_b32_e32 v249, 0xffff0000, v161
	v_pk_add_f32 v[230:231], v[230:231], v[232:233]
	v_pk_add_f32 v[234:235], v[234:235], v[236:237]
	v_pk_add_f32 v[238:239], v[238:239], v[240:241]
	v_pk_add_f32 v[242:243], v[242:243], v[244:245]
	v_pk_add_f32 v[230:231], v[230:231], v[234:235]
	v_pk_add_f32 v[238:239], v[238:239], v[242:243]
	v_pk_fma_f32 v[218:219], v[90:91], v[230:231], v[246:247]
	v_pk_fma_f32 v[220:221], v[92:93], v[238:239], v[248:249]
	v_pk_fma_f32 v[250:251], v[218:219], v[218:219], v[250:251]
	v_pk_fma_f32 v[250:251], v[220:221], v[220:221], v[250:251]
	v_cvt_pk_f32_fp8_e32 v[230:231], v184
	v_cvt_pk_f32_fp8_sdwa v[238:239], v184 src0_sel:WORD_1
	v_cvt_pk_f32_fp8_e32 v[232:233], v188
	v_cvt_pk_f32_fp8_sdwa v[240:241], v188 src0_sel:WORD_1
	v_cvt_pk_f32_fp8_e32 v[234:235], v192
	v_cvt_pk_f32_fp8_sdwa v[242:243], v192 src0_sel:WORD_1
	v_cvt_pk_f32_fp8_e32 v[236:237], v196
	v_cvt_pk_f32_fp8_sdwa v[244:245], v196 src0_sel:WORD_1
	v_lshlrev_b32_e32 v246, 16, v162
	v_and_b32_e32 v247, 0xffff0000, v162
	v_lshlrev_b32_e32 v248, 16, v163
	v_and_b32_e32 v249, 0xffff0000, v163
	v_pk_add_f32 v[230:231], v[230:231], v[232:233]
	v_pk_add_f32 v[234:235], v[234:235], v[236:237]
	v_pk_add_f32 v[238:239], v[238:239], v[240:241]
	v_pk_add_f32 v[242:243], v[242:243], v[244:245]
	v_pk_add_f32 v[230:231], v[230:231], v[234:235]
	v_pk_add_f32 v[238:239], v[238:239], v[242:243]
	v_pk_fma_f32 v[222:223], v[94:95], v[230:231], v[246:247]
	v_pk_fma_f32 v[224:225], v[96:97], v[238:239], v[248:249]
	v_pk_fma_f32 v[250:251], v[222:223], v[222:223], v[250:251]
	v_pk_fma_f32 v[250:251], v[224:225], v[224:225], v[250:251]
	v_cvt_pk_f32_fp8_e32 v[230:231], v185
	v_cvt_pk_f32_fp8_sdwa v[238:239], v185 src0_sel:WORD_1
	v_cvt_pk_f32_fp8_e32 v[232:233], v189
	v_cvt_pk_f32_fp8_sdwa v[240:241], v189 src0_sel:WORD_1
	v_cvt_pk_f32_fp8_e32 v[234:235], v193
	v_cvt_pk_f32_fp8_sdwa v[242:243], v193 src0_sel:WORD_1
	v_cvt_pk_f32_fp8_e32 v[236:237], v197
	v_cvt_pk_f32_fp8_sdwa v[244:245], v197 src0_sel:WORD_1
	v_lshlrev_b32_e32 v246, 16, v164
	v_and_b32_e32 v247, 0xffff0000, v164
	v_lshlrev_b32_e32 v248, 16, v165
	v_and_b32_e32 v249, 0xffff0000, v165
	v_pk_add_f32 v[230:231], v[230:231], v[232:233]
	v_pk_add_f32 v[234:235], v[234:235], v[236:237]
	v_pk_add_f32 v[238:239], v[238:239], v[240:241]
	v_pk_add_f32 v[242:243], v[242:243], v[244:245]
	v_pk_add_f32 v[230:231], v[230:231], v[234:235]
	v_pk_add_f32 v[238:239], v[238:239], v[242:243]
	v_pk_fma_f32 v[226:227], v[98:99], v[230:231], v[246:247]
	v_pk_fma_f32 v[228:229], v[100:101], v[238:239], v[248:249]
	v_pk_fma_f32 v[250:251], v[226:227], v[226:227], v[250:251]
	v_pk_fma_f32 v[250:251], v[228:229], v[228:229], v[250:251]
	s_nop 0
	v_add_f32_e32 v69, v250, v251
	ds_bpermute_b32 v230, v60, v69
	s_waitcnt lgkmcnt(0)
	v_add_f32_e32 v69, v69, v230
	ds_bpermute_b32 v230, v61, v69
	s_waitcnt lgkmcnt(0)
	v_add_f32_e32 v69, v69, v230
	ds_bpermute_b32 v230, v62, v69
	s_waitcnt lgkmcnt(0)
	v_add_f32_e32 v69, v69, v230
	ds_bpermute_b32 v230, v63, v69
	s_waitcnt lgkmcnt(0)
	v_add_f32_e32 v69, v69, v230
	ds_bpermute_b32 v230, v64, v69
	s_waitcnt lgkmcnt(0)
	v_add_f32_e32 v69, v69, v230
	ds_bpermute_b32 v230, v65, v69
	s_waitcnt lgkmcnt(0)
	v_add_f32_e32 v69, v69, v230
	v_fmamk_f32 v69, v69, 0x3a000000, v67
	v_mul_f32_e32 v230, 0x4f800000, v69
	v_cmp_gt_f32_e32 vcc, s3, v69
	s_nop 1
	v_cndmask_b32_e32 v69, v69, v230, vcc
	v_sqrt_f32_e32 v230, v69
	s_nop 0
	v_add_u32_e32 v231, -1, v230
	v_add_u32_e32 v232, 1, v230
	v_fma_f32 v233, -v231, v230, v69
	v_fma_f32 v234, -v232, v230, v69
	v_cmp_ge_f32_e64 s[0:1], 0, v233
	s_nop 1
	v_cndmask_b32_e64 v230, v230, v231, s[0:1]
	v_cmp_lt_f32_e64 s[0:1], 0, v234
	s_nop 1
	v_cndmask_b32_e64 v230, v230, v232, s[0:1]
	v_mul_f32_e32 v231, 0x37800000, v230
	v_cndmask_b32_e32 v230, v230, v231, vcc
	v_cmp_class_f32_e32 vcc, v69, v68
	s_nop 1
	v_cndmask_b32_e32 v69, v230, v69, vcc
	v_div_scale_f32 v230, s[0:1], v69, v69, 1.0
	v_rcp_f32_e32 v232, v230
	v_div_scale_f32 v231, vcc, 1.0, v69, 1.0
	v_fma_f32 v233, -v230, v232, 1.0
	v_fmac_f32_e32 v232, v233, v232
	v_mul_f32_e32 v233, v231, v232
	v_fma_f32 v234, -v230, v233, v231
	v_fmac_f32_e32 v233, v234, v232
	v_fma_f32 v230, -v230, v233, v231
	v_div_fmas_f32 v230, v230, v232, v233
	v_div_fixup_f32 v230, v230, v69, 1.0
	v_pk_mul_f32 v[198:199], v[198:199], v[230:231] op_sel_hi:[1,0]
	v_pk_mul_f32 v[200:201], v[200:201], v[230:231] op_sel_hi:[1,0]
	v_pk_mul_f32 v[202:203], v[202:203], v[230:231] op_sel_hi:[1,0]
	v_pk_mul_f32 v[204:205], v[204:205], v[230:231] op_sel_hi:[1,0]
	v_pk_mul_f32 v[206:207], v[206:207], v[230:231] op_sel_hi:[1,0]
	v_pk_mul_f32 v[208:209], v[208:209], v[230:231] op_sel_hi:[1,0]
	v_pk_mul_f32 v[210:211], v[210:211], v[230:231] op_sel_hi:[1,0]
	v_pk_mul_f32 v[212:213], v[212:213], v[230:231] op_sel_hi:[1,0]
	v_pk_mul_f32 v[214:215], v[214:215], v[230:231] op_sel_hi:[1,0]
	v_pk_mul_f32 v[216:217], v[216:217], v[230:231] op_sel_hi:[1,0]
	v_pk_mul_f32 v[218:219], v[218:219], v[230:231] op_sel_hi:[1,0]
	v_pk_mul_f32 v[220:221], v[220:221], v[230:231] op_sel_hi:[1,0]
	v_pk_mul_f32 v[222:223], v[222:223], v[230:231] op_sel_hi:[1,0]
	v_pk_mul_f32 v[224:225], v[224:225], v[230:231] op_sel_hi:[1,0]
	v_pk_mul_f32 v[226:227], v[226:227], v[230:231] op_sel_hi:[1,0]
	v_pk_mul_f32 v[228:229], v[228:229], v[230:231] op_sel_hi:[1,0]
	v_pk_mul_f32 v[198:199], v[0:1], v[198:199]
	v_pk_mul_f32 v[200:201], v[2:3], v[200:201]
	v_pk_mul_f32 v[202:203], v[4:5], v[202:203]
	v_pk_mul_f32 v[204:205], v[6:7], v[204:205]
	v_pk_mul_f32 v[206:207], v[8:9], v[206:207]
	v_pk_mul_f32 v[208:209], v[10:11], v[208:209]
	v_pk_mul_f32 v[210:211], v[12:13], v[210:211]
	v_pk_mul_f32 v[212:213], v[14:15], v[212:213]
	v_pk_mul_f32 v[214:215], v[16:17], v[214:215]
	v_pk_mul_f32 v[216:217], v[18:19], v[216:217]
	v_pk_mul_f32 v[218:219], v[20:21], v[218:219]
	v_pk_mul_f32 v[220:221], v[22:23], v[220:221]
	v_pk_mul_f32 v[222:223], v[24:25], v[222:223]
	v_pk_mul_f32 v[224:225], v[26:27], v[224:225]
	v_pk_mul_f32 v[226:227], v[28:29], v[226:227]
	v_pk_mul_f32 v[228:229], v[30:31], v[228:229]
	global_store_dwordx4 v[56:57], v[198:201], off
	global_store_dwordx4 v[56:57], v[202:205], off offset:16
	global_store_dwordx4 v[56:57], v[206:209], off offset:32
	global_store_dwordx4 v[56:57], v[210:213], off offset:48
	global_store_dwordx4 v[58:59], v[214:217], off
	global_store_dwordx4 v[58:59], v[218:221], off offset:16
	global_store_dwordx4 v[58:59], v[222:225], off offset:32
	global_store_dwordx4 v[58:59], v[226:229], off offset:48
	v_lshl_add_u64 v[56:57], v[56:57], 0, s[10:11]
	s_add_i32 s2, s2, s4
	s_cmp_lt_i32 s2, 0x8000
	s_cbranch_scc1 .Lp8_top
.Lp8_done:
	s_waitcnt vmcnt(0)
.LBB0_1121:
	s_endpgm
